# speedup vs baseline: 1.1014x; 1.0027x over previous
_Z10agg_kernelPKDF16_PKiS2_S2_PKfS2_PDF16_Pfi:
	s_load_dwordx8 s[12:19], s[0:1], 0x0
	s_lshl_b32 s4, s2, 1
	s_ashr_i32 s5, s4, 31
	s_lshl_b64 s[4:5], s[4:5], 2
	v_and_b32_e32 v1, 63, v0
	s_waitcnt lgkmcnt(0)
	s_add_u32 s20, s16, s4
	s_addc_u32 s21, s17, s5
	s_load_dwordx2 s[16:17], s[20:21], 0x0
	s_load_dwordx8 s[4:11], s[0:1], 0x20
	v_mov_b32_e32 v8, 0
	v_mov_b32_e32 v9, 0
	v_mov_b32_e32 v10, 0
	v_mov_b32_e32 v11, 0
	v_lshlrev_b32_e32 v12, 4, v0
	v_add_u32_e32 v13, 0x10000, v12
	ds_write_b128 v12, v[8:11]
	ds_write_b128 v12, v[8:11] offset:16384
	ds_write_b128 v12, v[8:11] offset:32768
	ds_write_b128 v12, v[8:11] offset:49152
	ds_write_b128 v13, v[8:11]
	ds_write_b128 v13, v[8:11] offset:16384
	ds_write_b128 v13, v[8:11] offset:32768
	v_cmp_gt_u32_e32 vcc, 0x28c, v0
	s_and_saveexec_b64 s[40:41], vcc
	ds_write_b128 v13, v[8:11] offset:49152
	s_or_b64 exec, exec, s[40:41]
	v_readfirstlane_b32 s3, v0
	v_lshlrev_b32_e32 v2, 2, v1
	s_lshr_b32 s3, s3, 6
	s_waitcnt lgkmcnt(0)
	s_ashr_i32 s21, s16, 31
	s_mov_b32 s20, s16
	global_load_dword v3, v2, s[6:7]
	global_load_dword v4, v2, s[6:7] offset:256
	global_load_dword v6, v2, s[6:7] offset:512
	global_load_dword v5, v2, s[6:7] offset:768
	s_lshl_b64 s[6:7], s[20:21], 2
	s_add_u32 s6, s14, s6
	s_addc_u32 s7, s15, s7
	s_add_i32 s21, s17, 15
	s_ashr_i32 s21, s21, 4
	s_max_i32 s20, s21, 1
	s_add_i32 s20, s20, -1
	s_min_u32 s14, s3, s20
	s_bfe_u32 s44, s2, 0x10002
	s_mul_i32 s45, s44, s20
	s_lshl_b32 s44, s44, 1
	s_sub_i32 s44, 1, s44
	s_mul_i32 s14, s14, s44
	s_add_i32 s14, s14, s45
	s_lshl_b32 s30, s14, 4
	v_mov_b32_e32 v59, 0x30e0000
	v_bfe_u32 v2, v0, 4, 2
	v_lshlrev_b32_e32 v7, 2, v0
	s_lshl_b32 s14, s14, 6
	v_and_or_b32 v18, v7, 12, v2
	s_add_u32 s14, s6, s14
	s_addc_u32 s15, s7, 0
	v_lshlrev_b32_e32 v2, 2, v18
	global_load_dword v2, v2, s[14:15]
	v_lshlrev_b32_e32 v20, 2, v18
	s_waitcnt vmcnt(2)
	v_max3_i32 v3, v3, v4, v6
	v_mbcnt_lo_u32_b32 v4, -1, 0
	v_mbcnt_hi_u32_b32 v4, -1, v4
	v_and_b32_e32 v25, 64, v4
	s_waitcnt vmcnt(1)
	v_max3_i32 v3, v3, v5, 0
	v_add_u32_e32 v5, 64, v25
	v_xor_b32_e32 v6, 1, v4
	v_cmp_lt_i32_e32 vcc, v6, v5
	s_load_dword s16, s[0:1], 0x40
	s_mul_i32 s14, s2, 0x187
	v_cndmask_b32_e32 v6, v4, v6, vcc
	v_lshlrev_b32_e32 v6, 2, v6
	ds_bpermute_b32 v6, v6, v3
	s_waitcnt lgkmcnt(0)
	s_sub_i32 s15, s16, s14
	s_movk_i32 s0, 0x73
	s_cmp_gt_i32 s21, s3
	s_cselect_b64 s[22:23], -1, 0
	v_max_i32_e32 v3, v3, v6
	v_xor_b32_e32 v6, 2, v4
	v_cmp_lt_i32_e32 vcc, v6, v5
	v_mov_b32_e32 v29, 0
	v_mov_b32_e32 v27, 0
	v_cndmask_b32_e32 v6, v4, v6, vcc
	v_lshlrev_b32_e32 v6, 2, v6
	ds_bpermute_b32 v6, v6, v3
	v_mov_b32_e32 v28, 0
	v_mov_b32_e32 v26, 0
	v_mov_b32_e32 v21, 0
	s_waitcnt lgkmcnt(0)
	v_max_i32_e32 v3, v3, v6
	v_xor_b32_e32 v6, 4, v4
	v_cmp_lt_i32_e32 vcc, v6, v5
	v_cndmask_b32_e32 v6, v4, v6, vcc
	v_lshlrev_b32_e32 v6, 2, v6
	ds_bpermute_b32 v6, v6, v3
	s_waitcnt lgkmcnt(0)
	s_barrier
	v_max_i32_e32 v3, v3, v6
	v_xor_b32_e32 v6, 8, v4
	v_cmp_lt_i32_e32 vcc, v6, v5
	s_nop 1
	v_cndmask_b32_e32 v6, v4, v6, vcc
	v_lshlrev_b32_e32 v60, 2, v6
	ds_bpermute_b32 v6, v60, v3
	s_waitcnt lgkmcnt(0)
	v_max_i32_e32 v3, v3, v6
	v_xor_b32_e32 v6, 16, v4
	v_cmp_lt_i32_e32 vcc, v6, v5
	s_nop 1
	v_cndmask_b32_e32 v6, v4, v6, vcc
	v_lshlrev_b32_e32 v61, 2, v6
	ds_bpermute_b32 v6, v61, v3
	s_waitcnt lgkmcnt(0)
	v_max_i32_e32 v3, v3, v6
	v_xor_b32_e32 v6, 32, v4
	v_cmp_lt_i32_e32 vcc, v6, v5
	v_and_b32_e32 v5, 15, v0
	v_lshlrev_b32_e32 v24, 4, v5
	v_cndmask_b32_e32 v4, v4, v6, vcc
	v_lshlrev_b32_e32 v66, 2, v4
	ds_bpermute_b32 v4, v66, v3
	v_lshlrev_b32_e32 v23, 2, v5
	s_waitcnt lgkmcnt(0)
	v_max_i32_e32 v3, v3, v4
	v_lshrrev_b32_e32 v3, 23, v3
	v_mov_b32_e32 v4, 0x8b
	v_med3_u32 v3, v3, s0, v4
	s_sub_i32 s0, s21, s3
	s_add_i32 s0, s0, 15
	s_cmp_gt_u32 s0, 15
	s_cselect_b64 s[24:25], -1, 0
	v_lshlrev_b32_e32 v19, 23, v3
	s_and_b64 s[22:23], s[22:23], s[24:25]
	v_sub_u32_e32 v22, 0x84800000, v19
	s_waitcnt vmcnt(0)
	v_add_u32_e32 v33, s30, v18
	v_cmp_gt_i32_e64 s[28:29], s17, v33
	s_nop 1
	v_cndmask_b32_e64 v2, v59, v2, s[28:29]
	s_nop 1
	v_mov_b32_dpp v29, v2 row_newbcast:0 row_mask:0xf bank_mask:0xf
	v_mov_b32_dpp v27, v2 row_newbcast:1 row_mask:0xf bank_mask:0xf
	v_mov_b32_dpp v28, v2 row_newbcast:2 row_mask:0xf bank_mask:0xf
	v_mov_b32_dpp v26, v2 row_newbcast:3 row_mask:0xf bank_mask:0xf
	s_and_b64 vcc, exec, s[22:23]
	s_cbranch_vccz .LBB2_5
	s_lshr_b32 s21, s0, 4
	s_mov_b32 s1, 0
	s_mov_b32 s22, 0x1ffff00
	s_mov_b32 s23, 0x4b400000
	v_lshl_add_u64 v[20:21], s[6:7], 0, v[20:21]
	s_add_i32 s0, s3, 16
	s_mov_b32 s24, s0
	s_min_i32 s24, s24, s20
	s_mul_i32 s24, s24, s44
	s_add_i32 s24, s24, s45
	s_lshl_b32 s24, s24, 4
	s_ashr_i32 s25, s24, 31
	v_lshl_add_u64 v[32:33], s[24:25], 2, v[20:21]
	global_load_dword v30, v[32:33], off
	v_lshlrev_b32_e32 v35, 8, v29
	v_and_or_b32 v35, v35, s22, v24
	global_load_dwordx4 v[2:5], v35, s[12:13]
	v_lshlrev_b32_e32 v35, 8, v27
	v_and_or_b32 v35, v35, s22, v24
	global_load_dwordx4 v[6:9], v35, s[12:13]
	v_lshlrev_b32_e32 v35, 8, v28
	v_and_or_b32 v35, v35, s22, v24
	global_load_dwordx4 v[10:13], v35, s[12:13]
	v_lshlrev_b32_e32 v35, 8, v26
	v_and_or_b32 v35, v35, s22, v24
	global_load_dwordx4 v[14:17], v35, s[12:13]
